# prologue de-serialisation: the grid barrier's first-use rendezvous loads its 16 per-XCD counters together and waits once (was one wait per load: 16 dependent round trips)
# baseline (speedup 1.0000x reference)
; __device__ __forceinline__ unsigned xb_ld(unsigned* p)              { return __hip_atomic_load(p, __ATOMIC_RELAXED, __HIP_MEMORY_SCOPE_AGENT); }
; __device__ __forceinline__ void xcd_barrier_complete(unsigned* bar, unsigned x, unsigned& nloc, unsigned& nx) {
;     const unsigned G = gridDim.x * gridDim.y * gridDim.z;
;     unsigned sum, cnt, mine, sp = 0u;
;     for (;;) {
;         sum = 0u; cnt = 0u; mine = 0u;
; #pragma unroll
;         for (unsigned j = 0; j < 16; ++j) { const unsigned c = xb_ld(&bar[XB_XCNT(j)]); sum += c; cnt += (c > 0u) ? 1u : 0u; mine = (j == x) ? c : mine; }
;         if (sum == G) break;
;         __builtin_amdgcn_s_sleep(1);
;         if ((++sp & 255u) == 0u) { if (xb_ld(&bar[XB_TMO])) break; if (sp > XB_SPIN_CAP) { atomicAdd(&bar[XB_TMO], 1u); break; } }
;     }
.LBB0_26:
	v_readlane_b32 s8, v253, 15
	v_readlane_b32 s9, v253, 16
	s_mov_b64 s[10:11], -1
	s_nop 3
	global_load_dword v2, v18, s[8:9] sc1
	v_readlane_b32 s8, v253, 17
	v_readlane_b32 s9, v253, 18
	s_nop 4
	global_load_dword v3, v18, s[8:9] sc1
	v_readlane_b32 s8, v253, 19
	v_readlane_b32 s9, v253, 20
	s_nop 4
	global_load_dword v4, v18, s[8:9] sc1
	v_readlane_b32 s8, v253, 21
	v_readlane_b32 s9, v253, 22
	s_nop 4
	global_load_dword v5, v18, s[8:9] sc1
	v_readlane_b32 s8, v253, 23
	v_readlane_b32 s9, v253, 24
	s_nop 4
	global_load_dword v6, v18, s[8:9] sc1
	v_readlane_b32 s8, v253, 25
	v_readlane_b32 s9, v253, 26
	s_nop 4
	global_load_dword v7, v18, s[8:9] sc1
	v_readlane_b32 s8, v253, 27
	v_readlane_b32 s9, v253, 28
	s_nop 4
	global_load_dword v8, v18, s[8:9] sc1
	v_readlane_b32 s8, v253, 29
	v_readlane_b32 s9, v253, 30
	s_nop 4
	global_load_dword v9, v18, s[8:9] sc1
	v_readlane_b32 s8, v253, 31
	v_readlane_b32 s9, v253, 32
	s_nop 4
	global_load_dword v10, v18, s[8:9] sc1
	v_readlane_b32 s8, v253, 33
	v_readlane_b32 s9, v253, 34
	s_nop 4
	global_load_dword v11, v18, s[8:9] sc1
	v_readlane_b32 s8, v253, 35
	v_readlane_b32 s9, v253, 36
	s_nop 4
	global_load_dword v12, v18, s[8:9] sc1
	v_readlane_b32 s8, v253, 37
	v_readlane_b32 s9, v253, 38
	s_nop 4
	global_load_dword v13, v18, s[8:9] sc1
	v_readlane_b32 s8, v253, 39
	v_readlane_b32 s9, v253, 40
	s_nop 4
	global_load_dword v14, v18, s[8:9] sc1
	v_readlane_b32 s8, v253, 41
	v_readlane_b32 s9, v253, 42
	s_nop 4
	global_load_dword v15, v18, s[8:9] sc1
	v_readlane_b32 s8, v253, 43
	v_readlane_b32 s9, v253, 44
	s_nop 4
	global_load_dword v16, v18, s[8:9] sc1
	v_readlane_b32 s8, v253, 45
	v_readlane_b32 s9, v253, 46
	s_nop 4
	global_load_dword v17, v18, s[8:9] sc1
	s_mov_b64 s[8:9], -1
	s_waitcnt vmcnt(0)
	v_add_u32_e32 v19, v3, v2
	v_add_u32_e32 v19, v19, v4
	v_add_u32_e32 v19, v19, v5
	v_add_u32_e32 v19, v19, v6
	v_add_u32_e32 v19, v19, v7
	v_add_u32_e32 v19, v19, v8
	v_add_u32_e32 v19, v19, v9
	v_add_u32_e32 v19, v19, v10
	v_add_u32_e32 v19, v19, v11
	v_add_u32_e32 v19, v19, v12
	v_add_u32_e32 v19, v19, v13
	v_add_u32_e32 v19, v19, v14
	v_add_u32_e32 v19, v19, v15
	v_add_u32_e32 v19, v19, v16
	v_add_u32_e32 v19, v19, v17
	v_cmp_eq_u32_e32 vcc, s15, v19
	s_cbranch_vccnz .LBB0_25
	s_and_b32 s8, s14, 0xff
	s_cmp_eq_u32 s8, 0
	s_mov_b64 s[8:9], -1
	s_mov_b64 s[12:13], -1
	s_sleep 1
	s_cbranch_scc1 .LBB0_30
	s_and_b64 vcc, exec, s[12:13]
	s_cbranch_vccz .LBB0_25

; __device__ __forceinline__ unsigned xb_ld(unsigned* p)              { return __hip_atomic_load(p, __ATOMIC_RELAXED, __HIP_MEMORY_SCOPE_AGENT); }
; __device__ __forceinline__ void xcd_barrier_complete(unsigned* bar, unsigned x, unsigned& nloc, unsigned& nx) {
;     const unsigned G = gridDim.x * gridDim.y * gridDim.z;
;     unsigned sum, cnt, mine, sp = 0u;
;     for (;;) {
;         sum = 0u; cnt = 0u; mine = 0u;
; #pragma unroll
;         for (unsigned j = 0; j < 16; ++j) { const unsigned c = xb_ld(&bar[XB_XCNT(j)]); sum += c; cnt += (c > 0u) ? 1u : 0u; mine = (j == x) ? c : mine; }
;         if (sum == G) break;
;         __builtin_amdgcn_s_sleep(1);
;         if ((++sp & 255u) == 0u) { if (xb_ld(&bar[XB_TMO])) break; if (sp > XB_SPIN_CAP) { atomicAdd(&bar[XB_TMO], 1u); break; } }
;     }
.LBB0_776:
	v_readlane_b32 s6, v253, 15
	v_readlane_b32 s7, v253, 16
	s_mov_b64 s[10:11], -1
	s_nop 3
	global_load_dword v1, v3, s[6:7] sc1
	v_readlane_b32 s6, v253, 17
	v_readlane_b32 s7, v253, 18
	s_nop 4
	global_load_dword v2, v3, s[6:7] sc1
	v_readlane_b32 s6, v253, 19
	v_readlane_b32 s7, v253, 20
	s_nop 4
	global_load_dword v4, v3, s[6:7] sc1
	v_readlane_b32 s6, v253, 21
	v_readlane_b32 s7, v253, 22
	s_nop 4
	global_load_dword v5, v3, s[6:7] sc1
	v_readlane_b32 s6, v253, 23
	v_readlane_b32 s7, v253, 24
	s_nop 4
	global_load_dword v6, v3, s[6:7] sc1
	v_readlane_b32 s6, v253, 25
	v_readlane_b32 s7, v253, 26
	s_nop 4
	global_load_dword v7, v3, s[6:7] sc1
	v_readlane_b32 s6, v253, 27
	v_readlane_b32 s7, v253, 28
	s_nop 4
	global_load_dword v8, v3, s[6:7] sc1
	v_readlane_b32 s6, v253, 29
	v_readlane_b32 s7, v253, 30
	s_nop 4
	global_load_dword v9, v3, s[6:7] sc1
	v_readlane_b32 s6, v253, 31
	v_readlane_b32 s7, v253, 32
	s_nop 4
	global_load_dword v10, v3, s[6:7] sc1
	v_readlane_b32 s6, v253, 33
	v_readlane_b32 s7, v253, 34
	s_nop 4
	global_load_dword v11, v3, s[6:7] sc1
	v_readlane_b32 s6, v253, 35
	v_readlane_b32 s7, v253, 36
	s_nop 4
	global_load_dword v12, v3, s[6:7] sc1
	v_readlane_b32 s6, v253, 37
	v_readlane_b32 s7, v253, 38
	s_nop 4
	global_load_dword v13, v3, s[6:7] sc1
	v_readlane_b32 s6, v253, 39
	v_readlane_b32 s7, v253, 40
	s_nop 4
	global_load_dword v14, v3, s[6:7] sc1
	v_readlane_b32 s6, v253, 41
	v_readlane_b32 s7, v253, 42
	s_nop 4
	global_load_dword v15, v3, s[6:7] sc1
	v_readlane_b32 s6, v253, 43
	v_readlane_b32 s7, v253, 44
	s_nop 4
	global_load_dword v16, v3, s[6:7] sc1
	v_readlane_b32 s6, v253, 45
	v_readlane_b32 s7, v253, 46
	s_nop 4
	global_load_dword v17, v3, s[6:7] sc1
	s_mov_b64 s[6:7], -1
	s_waitcnt vmcnt(0)
	v_add_u32_e32 v18, v2, v1
	v_add_u32_e32 v18, v18, v4
	v_add_u32_e32 v18, v18, v5
	v_add_u32_e32 v18, v18, v6
	v_add_u32_e32 v18, v18, v7
	v_add_u32_e32 v18, v18, v8
	v_add_u32_e32 v18, v18, v9
	v_add_u32_e32 v18, v18, v10
	v_add_u32_e32 v18, v18, v11
	v_add_u32_e32 v18, v18, v12
	v_add_u32_e32 v18, v18, v13
	v_add_u32_e32 v18, v18, v14
	v_add_u32_e32 v18, v18, v15
	v_add_u32_e32 v18, v18, v16
	v_add_u32_e32 v18, v18, v17
	v_cmp_eq_u32_e32 vcc, s3, v18
	s_cbranch_vccnz .LBB0_775
	s_and_b32 s6, s8, 0xff
	s_cmp_eq_u32 s6, 0
	s_mov_b64 s[6:7], -1
	s_mov_b64 s[12:13], -1
	s_sleep 1
	s_cbranch_scc1 .LBB0_780
	s_and_b64 vcc, exec, s[12:13]
	s_cbranch_vccz .LBB0_775

; __device__ __forceinline__ unsigned xb_ld(unsigned* p)              { return __hip_atomic_load(p, __ATOMIC_RELAXED, __HIP_MEMORY_SCOPE_AGENT); }
; __device__ __forceinline__ void xcd_barrier_complete(unsigned* bar, unsigned x, unsigned& nloc, unsigned& nx) {
;     const unsigned G = gridDim.x * gridDim.y * gridDim.z;
;     unsigned sum, cnt, mine, sp = 0u;
;     for (;;) {
;         sum = 0u; cnt = 0u; mine = 0u;
; #pragma unroll
;         for (unsigned j = 0; j < 16; ++j) { const unsigned c = xb_ld(&bar[XB_XCNT(j)]); sum += c; cnt += (c > 0u) ? 1u : 0u; mine = (j == x) ? c : mine; }
;         if (sum == G) break;
;         __builtin_amdgcn_s_sleep(1);
;         if ((++sp & 255u) == 0u) { if (xb_ld(&bar[XB_TMO])) break; if (sp > XB_SPIN_CAP) { atomicAdd(&bar[XB_TMO], 1u); break; } }
;     }
;     nloc = mine > 0u ? mine : 1u; nx = cnt > 0u ? cnt : 1u;
.LBB0_1420:
	v_readlane_b32 s4, v253, 15
	v_readlane_b32 s5, v253, 16
	s_mov_b64 s[6:7], -1
	s_nop 3
	global_load_dword v1, v3, s[4:5] sc1
	v_readlane_b32 s4, v253, 17
	v_readlane_b32 s5, v253, 18
	s_nop 4
	global_load_dword v2, v3, s[4:5] sc1
	v_readlane_b32 s4, v253, 19
	v_readlane_b32 s5, v253, 20
	s_nop 4
	global_load_dword v4, v3, s[4:5] sc1
	v_readlane_b32 s4, v253, 21
	v_readlane_b32 s5, v253, 22
	s_nop 4
	global_load_dword v5, v3, s[4:5] sc1
	v_readlane_b32 s4, v253, 23
	v_readlane_b32 s5, v253, 24
	s_nop 4
	global_load_dword v6, v3, s[4:5] sc1
	v_readlane_b32 s4, v253, 25
	v_readlane_b32 s5, v253, 26
	s_nop 4
	global_load_dword v7, v3, s[4:5] sc1
	v_readlane_b32 s4, v253, 27
	v_readlane_b32 s5, v253, 28
	s_nop 4
	global_load_dword v8, v3, s[4:5] sc1
	v_readlane_b32 s4, v253, 29
	v_readlane_b32 s5, v253, 30
	s_nop 4
	global_load_dword v9, v3, s[4:5] sc1
	v_readlane_b32 s4, v253, 31
	v_readlane_b32 s5, v253, 32
	s_nop 4
	global_load_dword v10, v3, s[4:5] sc1
	v_readlane_b32 s4, v253, 33
	v_readlane_b32 s5, v253, 34
	s_nop 4
	global_load_dword v11, v3, s[4:5] sc1
	v_readlane_b32 s4, v253, 35
	v_readlane_b32 s5, v253, 36
	s_nop 4
	global_load_dword v12, v3, s[4:5] sc1
	v_readlane_b32 s4, v253, 37
	v_readlane_b32 s5, v253, 38
	s_nop 4
	global_load_dword v13, v3, s[4:5] sc1
	v_readlane_b32 s4, v253, 39
	v_readlane_b32 s5, v253, 40
	s_nop 4
	global_load_dword v14, v3, s[4:5] sc1
	v_readlane_b32 s4, v253, 41
	v_readlane_b32 s5, v253, 42
	s_nop 4
	global_load_dword v15, v3, s[4:5] sc1
	v_readlane_b32 s4, v253, 43
	v_readlane_b32 s5, v253, 44
	s_nop 4
	global_load_dword v16, v3, s[4:5] sc1
	v_readlane_b32 s4, v253, 45
	v_readlane_b32 s5, v253, 46
	s_nop 4
	global_load_dword v17, v3, s[4:5] sc1
	s_mov_b64 s[4:5], -1
	s_waitcnt vmcnt(0)
	v_add_u32_e32 v18, v2, v1
	v_add_u32_e32 v18, v18, v4
	v_add_u32_e32 v18, v18, v5
	v_add_u32_e32 v18, v18, v6
	v_add_u32_e32 v18, v18, v7
	v_add_u32_e32 v18, v18, v8
	v_add_u32_e32 v18, v18, v9
	v_add_u32_e32 v18, v18, v10
	v_add_u32_e32 v18, v18, v11
	v_add_u32_e32 v18, v18, v12
	v_add_u32_e32 v18, v18, v13
	v_add_u32_e32 v18, v18, v14
	v_add_u32_e32 v18, v18, v15
	v_add_u32_e32 v18, v18, v16
	v_add_u32_e32 v18, v18, v17
	v_cmp_eq_u32_e32 vcc, s2, v18
	s_cbranch_vccnz .LBB0_1419
	s_and_b32 s4, s3, 0xff
	s_cmp_eq_u32 s4, 0
	s_mov_b64 s[4:5], -1
	s_mov_b64 s[12:13], -1
	s_sleep 1
	s_cbranch_scc1 .LBB0_1424
	s_and_b64 vcc, exec, s[12:13]
	s_cbranch_vccz .LBB0_1419

; __device__ __forceinline__ unsigned xb_ld(unsigned* p)              { return __hip_atomic_load(p, __ATOMIC_RELAXED, __HIP_MEMORY_SCOPE_AGENT); }
; __device__ __forceinline__ void xcd_barrier_complete(unsigned* bar, unsigned x, unsigned& nloc, unsigned& nx) {
;     const unsigned G = gridDim.x * gridDim.y * gridDim.z;
;     unsigned sum, cnt, mine, sp = 0u;
;     for (;;) {
;         sum = 0u; cnt = 0u; mine = 0u;
; #pragma unroll
;         for (unsigned j = 0; j < 16; ++j) { const unsigned c = xb_ld(&bar[XB_XCNT(j)]); sum += c; cnt += (c > 0u) ? 1u : 0u; mine = (j == x) ? c : mine; }
;         if (sum == G) break;
;         __builtin_amdgcn_s_sleep(1);
;         if ((++sp & 255u) == 0u) { if (xb_ld(&bar[XB_TMO])) break; if (sp > XB_SPIN_CAP) { atomicAdd(&bar[XB_TMO], 1u); break; } }
;     }
;     nloc = mine > 0u ? mine : 1u; nx = cnt > 0u ? cnt : 1u;
.LBB0_1504:
	v_readlane_b32 s6, v253, 15
	v_readlane_b32 s7, v253, 16
	s_mov_b64 s[12:13], -1
	s_nop 3
	global_load_dword v1, v3, s[6:7] sc1
	v_readlane_b32 s6, v253, 17
	v_readlane_b32 s7, v253, 18
	s_nop 4
	global_load_dword v2, v3, s[6:7] sc1
	v_readlane_b32 s6, v253, 19
	v_readlane_b32 s7, v253, 20
	s_nop 4
	global_load_dword v4, v3, s[6:7] sc1
	v_readlane_b32 s6, v253, 21
	v_readlane_b32 s7, v253, 22
	s_nop 4
	global_load_dword v5, v3, s[6:7] sc1
	v_readlane_b32 s6, v253, 23
	v_readlane_b32 s7, v253, 24
	s_nop 4
	global_load_dword v6, v3, s[6:7] sc1
	v_readlane_b32 s6, v253, 25
	v_readlane_b32 s7, v253, 26
	s_nop 4
	global_load_dword v7, v3, s[6:7] sc1
	v_readlane_b32 s6, v253, 27
	v_readlane_b32 s7, v253, 28
	s_nop 4
	global_load_dword v8, v3, s[6:7] sc1
	v_readlane_b32 s6, v253, 29
	v_readlane_b32 s7, v253, 30
	s_nop 4
	global_load_dword v9, v3, s[6:7] sc1
	v_readlane_b32 s6, v253, 31
	v_readlane_b32 s7, v253, 32
	s_nop 4
	global_load_dword v10, v3, s[6:7] sc1
	v_readlane_b32 s6, v253, 33
	v_readlane_b32 s7, v253, 34
	s_nop 4
	global_load_dword v11, v3, s[6:7] sc1
	v_readlane_b32 s6, v253, 35
	v_readlane_b32 s7, v253, 36
	s_nop 4
	global_load_dword v12, v3, s[6:7] sc1
	v_readlane_b32 s6, v253, 37
	v_readlane_b32 s7, v253, 38
	s_nop 4
	global_load_dword v13, v3, s[6:7] sc1
	v_readlane_b32 s6, v253, 39
	v_readlane_b32 s7, v253, 40
	s_nop 4
	global_load_dword v14, v3, s[6:7] sc1
	v_readlane_b32 s6, v253, 41
	v_readlane_b32 s7, v253, 42
	s_nop 4
	global_load_dword v15, v3, s[6:7] sc1
	v_readlane_b32 s6, v253, 43
	v_readlane_b32 s7, v253, 44
	s_nop 4
	global_load_dword v16, v3, s[6:7] sc1
	v_readlane_b32 s6, v253, 45
	v_readlane_b32 s7, v253, 46
	s_nop 4
	global_load_dword v17, v3, s[6:7] sc1
	s_mov_b64 s[6:7], -1
	s_waitcnt vmcnt(0)
	v_add_u32_e32 v18, v2, v1
	v_add_u32_e32 v18, v18, v4
	v_add_u32_e32 v18, v18, v5
	v_add_u32_e32 v18, v18, v6
	v_add_u32_e32 v18, v18, v7
	v_add_u32_e32 v18, v18, v8
	v_add_u32_e32 v18, v18, v9
	v_add_u32_e32 v18, v18, v10
	v_add_u32_e32 v18, v18, v11
	v_add_u32_e32 v18, v18, v12
	v_add_u32_e32 v18, v18, v13
	v_add_u32_e32 v18, v18, v14
	v_add_u32_e32 v18, v18, v15
	v_add_u32_e32 v18, v18, v16
	v_add_u32_e32 v18, v18, v17
	v_cmp_eq_u32_e32 vcc, s3, v18
	s_cbranch_vccnz .LBB0_1503
	s_and_b32 s6, s8, 0xff
	s_cmp_eq_u32 s6, 0
	s_mov_b64 s[6:7], -1
	s_mov_b64 s[14:15], -1
	s_sleep 1
	s_cbranch_scc1 .LBB0_1508
	s_and_b64 vcc, exec, s[14:15]
	s_cbranch_vccz .LBB0_1503
